# gather group-loop heads aligned to 64 bytes (instruction fetch phase)
# baseline (speedup 1.0000x reference)
.LBB0_762:
	v_ashrrev_i32_e32 v1, 31, v0
	v_lshlrev_b64 v[2:3], 6, v[0:1]
	v_lshl_add_u64 v[2:3], s[96:97], 0, v[2:3]
	v_mov_b64_e32 v[84:85], v[226:227]
	v_mov_b64_e32 v[86:87], v[228:229]
	v_mov_b64_e32 v[88:89], v[230:231]
	v_mov_b64_e32 v[90:91], v[232:233]
	v_lshlrev_b64 v[72:73], 11, v[0:1]
	v_mov_b64_e32 v[94:95], v[234:235]
	v_mov_b64_e32 v[96:97], v[236:237]
	v_lshl_add_u64 v[72:73], v[26:27], 0, v[72:73]
	v_mov_b64_e32 v[98:99], v[238:239]
	v_mov_b64_e32 v[100:101], v[240:241]
	v_mov_b64_e32 v[102:103], v[242:243]
	v_mov_b64_e32 v[104:105], v[244:245]
	v_mov_b64_e32 v[106:107], v[246:247]
	v_mov_b64_e32 v[108:109], v[248:249]
	v_add_u32_e32 v250, s86, v0
	v_cmp_gt_i32_e32 vcc, s87, v250
	s_nop 1
	v_cndmask_b32_e32 v250, v0, v250, vcc
	v_ashrrev_i32_e32 v251, 31, v250
	v_lshlrev_b64 v[250:251], 6, v[250:251]
	v_lshl_add_u64 v[4:5], s[96:97], 0, v[250:251]
	v_lshlrev_b64 v[250:251], 5, v[250:251]
	v_lshl_add_u64 v[250:251], v[26:27], 0, v[250:251]
	global_load_dwordx4 v[226:229], v[4:5], off
	global_load_dwordx4 v[230:233], v[4:5], off offset:16
	global_load_dwordx4 v[234:237], v[4:5], off offset:32
	global_load_dwordx4 v[238:241], v[250:251], off
	global_load_dwordx4 v[242:245], v[250:251], off offset:16
	global_load_dwordx4 v[246:249], v[4:5], off offset:48
	s_mov_b32 s14, 0x42ee0000
	s_mov_b32 s58, 16
	v_mov_b32_e32 v2, v85
	v_mov_b32_e32 v3, v86
	v_mov_b32_e32 v72, v89
	v_mov_b32_e32 v73, v90
	v_mov_b32_e32 v85, v87
	v_mov_b32_e32 v89, v91
	v_mov_b32_e32 v86, v95
	v_mov_b32_e32 v90, v97
	v_lshlrev_b32_e32 v91, 16, v98
	v_pk_add_f32 v[2:3], v[2:3], v[84:85]
	v_pk_add_f32 v[72:73], v[72:73], v[88:89]
	v_pk_add_f32 v[84:85], v[94:95], v[86:87]
	v_pk_add_f32 v[86:87], v[96:97], v[90:91]
	v_pk_add_f32 v[2:3], v[2:3], v[2:3] op_sel:[0,1] op_sel_hi:[1,0]
	v_pk_add_f32 v[72:73], v[72:73], v[72:73] op_sel:[0,1] op_sel_hi:[1,0]
	v_mov_b32_e32 v85, v108
	v_mov_b32_e32 v87, v109
	v_mov_b32_e32 v3, v106
	v_mov_b32_e32 v73, v107
	v_pk_add_f32 v[84:85], v[84:85], v[86:87]
	v_pk_add_f32 v[2:3], v[2:3], v[72:73]
	v_and_b32_e32 v98, 0xffff0000, v98
	v_pk_add_f32 v[2:3], v[2:3], v[84:85]
	v_lshlrev_b32_e32 v110, 16, v99
	v_add_f32_e32 v2, v2, v3
	v_fmamk_f32 v2, v2, 0x3a800000, v191
	v_mul_f32_e32 v3, 0x4b800000, v2
	v_cmp_gt_f32_e32 vcc, s18, v2
	v_and_b32_e32 v99, 0xffff0000, v99
	v_lshlrev_b32_e32 v111, 16, v100
	v_cndmask_b32_e32 v2, v2, v3, vcc
	v_rsq_f32_e32 v2, v2
	v_and_b32_e32 v100, 0xffff0000, v100
	v_lshlrev_b32_e32 v112, 16, v101
	v_and_b32_e32 v101, 0xffff0000, v101
	v_mul_f32_e32 v84, 0x45800000, v2
	v_cndmask_b32_e32 v2, v2, v84, vcc
	v_lshlrev_b32_e32 v113, 16, v102
	v_and_b32_e32 v102, 0xffff0000, v102
	v_lshlrev_b32_e32 v114, 16, v103
	v_and_b32_e32 v103, 0xffff0000, v103
	v_lshlrev_b32_e32 v115, 16, v104
	v_and_b32_e32 v3, 0xffff0000, v104
	v_lshlrev_b32_e32 v72, 16, v105
	v_and_b32_e32 v73, 0xffff0000, v105
	v_mul_f32_e32 v84, v2, v91
	v_mul_f32_e32 v85, v2, v98
	v_mul_f32_e32 v86, v2, v110
	v_mul_f32_e32 v87, v2, v99
	v_mul_f32_e32 v88, v2, v111
	v_mul_f32_e32 v89, v2, v100
	v_mul_f32_e32 v90, v2, v112
	v_mul_f32_e32 v91, v2, v101
	v_mul_f32_e32 v95, v2, v113
	v_mul_f32_e32 v96, v2, v102
	v_mul_f32_e32 v97, v2, v114
	v_mul_f32_e32 v98, v2, v103
	v_mul_f32_e32 v99, v2, v115
	v_mul_f32_e32 v100, v2, v3
	v_mul_f32_e32 v72, v2, v72
	v_mul_f32_e32 v73, v2, v73
	v_max_f32_e64 v2, |v84|, |v85|
	v_max_f32_e64 v3, |v86|, |v87|
	v_max_f32_e64 v94, |v88|, |v89|
	v_max_f32_e64 v101, |v90|, |v91|
	v_max3_f32 v2, v2, 0, v3
	v_max_f32_e64 v102, |v95|, |v96|
	v_max_f32_e64 v103, |v97|, |v98|
	v_max3_f32 v2, v2, v94, v101
	v_max_f32_e64 v104, |v99|, |v100|
	v_max_f32_e64 v105, |v72|, |v73|
	v_max3_f32 v2, v2, v102, v103
	v_max3_f32 v2, v2, v104, v105
	v_mov_b32_e32 v3, v2
	s_nop 1
	v_permlane32_swap_b32 v3, v2
	v_add_u32_e32 v94, s86, v0
	v_cmp_gt_i32_e64 s[48:49], s87, v94
	s_waitcnt lgkmcnt(0)
	v_max_f32_e32 v3, v3, v3
	v_max_f32_e32 v2, v2, v3
	v_mov_b32_e32 v3, v2
	s_nop 1
	v_permlane16_swap_b32 v3, v2
	s_waitcnt lgkmcnt(0)
	v_max_f32_e32 v3, v3, v3
	v_max_f32_e32 v2, v2, v3
	s_nop 1
	v_mov_b32_dpp v3, v2 row_ror:8 row_mask:0xf bank_mask:0xf
	s_waitcnt lgkmcnt(0)
	v_max_f32_e32 v3, v3, v3
	v_max_f32_e32 v2, v2, v3
	s_nop 1
	v_mov_b32_dpp v3, v2 row_half_mirror row_mask:0xf bank_mask:0xf
	s_nop 1
	v_mov_b32_dpp v3, v3 quad_perm:[3,2,1,0] row_mask:0xf bank_mask:0xf
	s_waitcnt lgkmcnt(0)
	v_max_f32_e32 v3, v3, v3
	v_max_f32_e32 v2, v2, v3
	s_nop 1
	v_mov_b32_dpp v3, v2 quad_perm:[2,3,0,1] row_mask:0xf bank_mask:0xf
	s_waitcnt lgkmcnt(0)
	v_max_f32_e32 v3, v3, v3
	v_max_f32_e32 v101, v2, v3
	s_nop 1
	v_mov_b32_dpp v102, v101 quad_perm:[1,0,3,2] row_mask:0xf bank_mask:0xf
	v_lshlrev_b64 v[2:3], 10, v[0:1]
	v_lshlrev_b64 v[206:207], 2, v[2:3]
	v_lshl_add_u64 v[206:207], v[28:29], 0, v[206:207]
	global_load_dwordx4 v[208:211], v[206:207], off offset:48
	global_load_dwordx4 v[212:215], v[206:207], off offset:32
	global_load_dwordx4 v[216:219], v[206:207], off offset:16
	global_load_dwordx4 v[220:223], v[206:207], off
	s_waitcnt lgkmcnt(0)
	v_max_f32_e32 v1, v102, v102
	v_max_f32_e32 v101, v101, v1
	v_div_scale_f32 v1, s[12:13], v101, v101, s14
	v_rcp_f32_e32 v102, v1
	v_div_scale_f32 v103, vcc, s14, v101, s14
	s_movk_i32 s12, 0x3fff
	v_fma_f32 v104, -v1, v102, 1.0
	v_fmac_f32_e32 v102, v104, v102
	v_mul_f32_e32 v104, v103, v102
	v_fma_f32 v105, -v1, v104, v103
	v_fmac_f32_e32 v104, v105, v102
	v_fma_f32 v1, -v1, v104, v103
	v_div_fmas_f32 v1, v1, v102, v104
	v_div_fixup_f32 v1, v1, v101, s14
	v_cmp_lt_f32_e32 vcc, 0, v101
	v_cmp_lt_i32_e64 s[50:51], s12, v94
	s_or_b64 s[10:11], s[50:51], s[10:11]
	v_cndmask_b32_e32 v102, 0, v1, vcc
	v_mul_f32_e32 v1, v84, v102
	v_mul_f32_e32 v84, v85, v102
	v_mul_f32_e32 v85, v86, v102
	v_mul_f32_e32 v86, v87, v102
	v_rndne_f32_e32 v1, v1
	v_rndne_f32_e32 v84, v84
	v_mul_f32_e32 v87, v88, v102
	v_mul_f32_e32 v88, v89, v102
	v_rndne_f32_e32 v85, v85
	v_rndne_f32_e32 v86, v86
	v_cvt_i32_f32_e32 v1, v1
	v_cvt_i32_f32_e32 v84, v84
	v_rndne_f32_e32 v87, v87
	v_rndne_f32_e32 v88, v88
	v_cvt_i32_f32_e32 v85, v85
	v_cvt_i32_f32_e32 v86, v86
	v_cvt_i32_f32_e32 v87, v87
	v_cvt_i32_f32_e32 v88, v88
	v_mul_f32_e32 v89, v90, v102
	v_add_u32_e32 v90, 8, v1
	v_add_u32_e32 v104, 8, v84
	v_and_b32_e32 v103, 15, v1
	v_lshlrev_b32_e32 v105, 4, v84
	v_add_u32_e32 v1, v1, v84
	v_lshl_add_u32 v84, v85, 4, v196
	v_lshl_add_u32 v107, v86, 8, v200
	v_lshrrev_b32_e32 v90, 4, v90
	v_and_b32_e32 v104, 0xf0, v104
	v_lshl_add_u32 v109, v87, 12, v201
	v_lshl_add_u32 v111, v88, 16, v202
	v_and_b32_e32 v84, 0xf00, v84
	v_and_b32_e32 v107, 0xf000, v107
	v_and_or_b32 v90, v90, 15, v104
	v_lshlrev_b32_e32 v106, 8, v85
	v_add3_u32 v1, v1, v85, v86
	v_and_b32_e32 v85, 0xf0000, v109
	v_and_b32_e32 v109, 0xf00000, v111
	v_or3_b32 v84, v90, v84, v107
	v_lshlrev_b32_e32 v110, 16, v87
	v_or3_b32 v84, v84, v85, v109
	v_add3_u32 v85, v1, v87, v88
	v_mul_f32_e32 v87, v91, v102
	v_rndne_f32_e32 v89, v89
	v_rndne_f32_e32 v87, v87
	v_cvt_i32_f32_e32 v89, v89
	v_cvt_i32_f32_e32 v87, v87
	v_lshlrev_b32_e32 v108, 12, v86
	v_and_b32_e32 v105, 0xf0, v105
	v_lshl_add_u32 v1, v89, 20, v203
	v_lshl_add_u32 v90, v87, 24, v204
	v_and_b32_e32 v1, 0xf000000, v1
	v_and_b32_e32 v90, 0xf0000000, v90
	v_and_b32_e32 v106, 0xf00, v106
	v_or3_b32 v1, v84, v1, v90
	v_lshl_or_b32 v84, v87, 28, v103
	v_lshlrev_b32_e32 v112, 20, v88
	v_and_b32_e32 v108, 0xf000, v108
	v_and_b32_e32 v86, 0xf0000, v110
	v_lshlrev_b32_e32 v88, 24, v89
	v_or3_b32 v84, v84, v105, v106
	v_and_b32_e32 v110, 0xf00000, v112
	v_and_b32_e32 v88, 0xf000000, v88
	v_or3_b32 v84, v84, v108, v86
	v_or3_b32 v88, v84, v110, v88
	v_add3_u32 v84, v85, v89, v87
	v_mul_f32_e32 v85, v95, v102
	v_mul_f32_e32 v86, v96, v102
	v_rndne_f32_e32 v85, v85
	v_rndne_f32_e32 v86, v86
	v_cvt_i32_f32_e32 v85, v85
	v_cvt_i32_f32_e32 v86, v86
	v_mul_f32_e32 v95, v99, v102
	v_mul_f32_e32 v96, v100, v102
	v_add_u32_e32 v87, 8, v85
	v_add_u32_e32 v89, 8, v86
	v_lshrrev_b32_e32 v87, 4, v87
	v_and_b32_e32 v89, 0xf0, v89
	v_and_or_b32 v87, v87, 15, v89
	v_mul_f32_e32 v89, v97, v102
	v_lshlrev_b32_e32 v91, 4, v86
	v_add3_u32 v84, v84, v85, v86
	v_mul_f32_e32 v86, v98, v102
	v_rndne_f32_e32 v89, v89
	v_rndne_f32_e32 v86, v86
	v_cvt_i32_f32_e32 v89, v89
	v_cvt_i32_f32_e32 v86, v86
	v_rndne_f32_e32 v95, v95
	v_rndne_f32_e32 v96, v96
	v_mul_f32_e32 v72, v72, v102
	v_mul_f32_e32 v73, v73, v102
	v_cvt_i32_f32_e32 v95, v95
	v_cvt_i32_f32_e32 v96, v96
	v_rndne_f32_e32 v72, v72
	v_rndne_f32_e32 v73, v73
	v_cvt_i32_f32_e32 v72, v72
	v_cvt_i32_f32_e32 v73, v73
	v_add3_u32 v84, v84, v89, v86
	v_add3_u32 v84, v84, v95, v96
	v_and_b32_e32 v90, 15, v85
	v_add3_u32 v84, v84, v72, v73
	v_cvt_f32_i32_e32 v84, v84
	v_lshl_add_u32 v85, v89, 4, v196
	v_lshlrev_b32_e32 v89, 8, v89
	v_and_b32_e32 v97, 0xf00, v89
	v_mov_b32_e32 v98, v84
	s_nop 1
	v_permlane32_swap_b32 v98, v84
	v_lshl_add_u32 v89, v86, 8, v200
	v_and_b32_e32 v85, 0xf00, v85
	v_and_b32_e32 v89, 0xf000, v89
	v_or3_b32 v85, v87, v85, v89
	s_waitcnt lgkmcnt(0)
	v_add_f32_e32 v84, v98, v84
	v_mov_b32_e32 v87, v84
	s_nop 1
	v_permlane16_swap_b32 v87, v84
	v_lshl_add_u32 v89, v95, 12, v201
	v_lshl_add_u32 v98, v96, 16, v202
	v_and_b32_e32 v89, 0xf0000, v89
	v_and_b32_e32 v98, 0xf00000, v98
	s_waitcnt lgkmcnt(0)
	v_add_f32_e32 v84, v84, v87
	s_nop 1
	v_mov_b32_dpp v87, v84 row_ror:8 row_mask:0xf bank_mask:0xf
	v_or3_b32 v85, v85, v89, v98
	v_lshlrev_b32_e32 v89, 20, v96
	v_and_b32_e32 v96, 0xf00000, v89
	v_lshl_add_u32 v89, v72, 20, v203
	s_waitcnt lgkmcnt(0)
	v_add_f32_e32 v84, v84, v87
	s_nop 1
	v_mov_b32_dpp v87, v84 row_half_mirror row_mask:0xf bank_mask:0xf
	s_nop 1
	v_mov_b32_dpp v87, v87 quad_perm:[3,2,1,0] row_mask:0xf bank_mask:0xf
	v_lshl_add_u32 v98, v73, 24, v204
	v_and_b32_e32 v89, 0xf000000, v89
	v_and_b32_e32 v98, 0xf0000000, v98
	v_or3_b32 v89, v85, v89, v98
	s_waitcnt lgkmcnt(0)
	v_add_f32_e32 v84, v84, v87
	s_nop 1
	v_mov_b32_dpp v87, v84 quad_perm:[2,3,0,1] row_mask:0xf bank_mask:0xf
	v_and_b32_e32 v91, 0xf0, v91
	v_lshlrev_b32_e32 v86, 12, v86
	v_lshlrev_b32_e32 v95, 16, v95
	v_lshl_or_b32 v73, v73, 28, v90
	s_waitcnt lgkmcnt(0)
	v_add_f32_e32 v84, v84, v87
	s_nop 1
	v_mov_b32_dpp v85, v84 quad_perm:[1,0,3,2] row_mask:0xf bank_mask:0xf
	v_and_b32_e32 v86, 0xf000, v86
	v_and_b32_e32 v95, 0xf0000, v95
	v_lshlrev_b32_e32 v72, 24, v72
	v_or3_b32 v73, v73, v91, v97
	v_and_b32_e32 v72, 0xf000000, v72
	v_or3_b32 v73, v73, v86, v95
	v_or3_b32 v90, v73, v96, v72
	s_waitcnt lgkmcnt(0)
	v_add_f32_e32 v72, v84, v85
	v_mul_f32_e32 v91, 0x3c09ae41, v101
	v_mul_f32_e32 v95, 0.5, v72
	v_mov_b32_e32 v103, 0
	v_mov_b64_e32 v[72:73], v[34:35]
	v_mov_b32_e32 v102, 0
	v_mov_b32_e32 v101, 0
	v_mov_b32_e32 v100, 0
	v_mov_b32_e32 v99, 0
	v_mov_b32_e32 v98, 0
	v_mov_b32_e32 v97, 0
	v_mov_b32_e32 v96, 0
	.p2align 6

.LBB0_769:
	v_ashrrev_i32_e32 v1, 31, v0
	v_lshlrev_b64 v[2:3], 6, v[0:1]
	v_lshl_add_u64 v[14:15], s[96:97], 0, v[2:3]
	v_mov_b64_e32 v[2:3], v[226:227]
	v_mov_b64_e32 v[4:5], v[228:229]
	v_mov_b64_e32 v[6:7], v[230:231]
	v_mov_b64_e32 v[8:9], v[232:233]
	v_lshlrev_b64 v[74:75], 11, v[0:1]
	v_mov_b64_e32 v[10:11], v[234:235]
	v_mov_b64_e32 v[12:13], v[236:237]
	v_lshl_add_u64 v[74:75], v[42:43], 0, v[74:75]
	v_mov_b64_e32 v[98:99], v[238:239]
	v_mov_b64_e32 v[100:101], v[240:241]
	v_mov_b64_e32 v[102:103], v[242:243]
	v_mov_b64_e32 v[104:105], v[244:245]
	v_mov_b64_e32 v[106:107], v[246:247]
	v_mov_b64_e32 v[108:109], v[248:249]
	v_add_u32_e32 v250, s86, v0
	v_cmp_gt_i32_e32 vcc, s87, v250
	s_nop 1
	v_cndmask_b32_e32 v250, v0, v250, vcc
	v_ashrrev_i32_e32 v251, 31, v250
	v_lshlrev_b64 v[250:251], 6, v[250:251]
	v_lshl_add_u64 v[16:17], s[96:97], 0, v[250:251]
	v_lshlrev_b64 v[250:251], 5, v[250:251]
	v_lshl_add_u64 v[250:251], v[42:43], 0, v[250:251]
	global_load_dwordx4 v[226:229], v[16:17], off
	global_load_dwordx4 v[230:233], v[16:17], off offset:16
	global_load_dwordx4 v[234:237], v[16:17], off offset:32
	global_load_dwordx4 v[238:241], v[250:251], off
	global_load_dwordx4 v[242:245], v[250:251], off offset:16
	global_load_dwordx4 v[246:249], v[16:17], off offset:48
	s_mov_b32 s56, 16
	v_mov_b32_e32 v14, v3
	v_mov_b32_e32 v15, v4
	v_mov_b32_e32 v94, v7
	v_mov_b32_e32 v95, v8
	v_mov_b32_e32 v3, v5
	v_mov_b32_e32 v7, v9
	v_mov_b32_e32 v4, v11
	v_mov_b32_e32 v8, v13
	v_pk_add_f32 v[2:3], v[14:15], v[2:3]
	v_pk_add_f32 v[6:7], v[94:95], v[6:7]
	v_pk_add_f32 v[4:5], v[10:11], v[4:5]
	v_pk_add_f32 v[8:9], v[12:13], v[8:9]
	v_pk_add_f32 v[2:3], v[2:3], v[2:3] op_sel:[0,1] op_sel_hi:[1,0]
	v_pk_add_f32 v[6:7], v[6:7], v[6:7] op_sel:[0,1] op_sel_hi:[1,0]
	v_mov_b32_e32 v5, v108
	v_mov_b32_e32 v9, v109
	v_mov_b32_e32 v3, v106
	v_mov_b32_e32 v7, v107
	v_pk_add_f32 v[4:5], v[4:5], v[8:9]
	v_pk_add_f32 v[2:3], v[2:3], v[6:7]
	v_lshlrev_b32_e32 v110, 16, v98
	v_pk_add_f32 v[2:3], v[2:3], v[4:5]
	v_and_b32_e32 v98, 0xffff0000, v98
	v_add_f32_e32 v2, v2, v3
	v_fmamk_f32 v2, v2, 0x3a800000, v191
	v_mul_f32_e32 v3, 0x4b800000, v2
	v_cmp_gt_f32_e32 vcc, s12, v2
	v_lshlrev_b32_e32 v111, 16, v99
	v_and_b32_e32 v99, 0xffff0000, v99
	v_cndmask_b32_e32 v2, v2, v3, vcc
	v_rsq_f32_e32 v2, v2
	v_lshlrev_b32_e32 v112, 16, v100
	v_and_b32_e32 v100, 0xffff0000, v100
	v_lshlrev_b32_e32 v113, 16, v101
	v_mul_f32_e32 v6, 0x45800000, v2
	v_cndmask_b32_e32 v2, v2, v6, vcc
	v_and_b32_e32 v101, 0xffff0000, v101
	v_lshlrev_b32_e32 v114, 16, v102
	v_and_b32_e32 v102, 0xffff0000, v102
	v_lshlrev_b32_e32 v115, 16, v103
	v_and_b32_e32 v103, 0xffff0000, v103
	v_lshlrev_b32_e32 v116, 16, v104
	v_and_b32_e32 v3, 0xffff0000, v104
	v_lshlrev_b32_e32 v4, 16, v105
	v_and_b32_e32 v5, 0xffff0000, v105
	v_mul_f32_e32 v6, v2, v110
	v_mul_f32_e32 v7, v2, v98
	v_mul_f32_e32 v8, v2, v111
	v_mul_f32_e32 v9, v2, v99
	v_mul_f32_e32 v10, v2, v112
	v_mul_f32_e32 v11, v2, v100
	v_mul_f32_e32 v12, v2, v113
	v_mul_f32_e32 v13, v2, v101
	v_mul_f32_e32 v14, v2, v114
	v_mul_f32_e32 v15, v2, v102
	v_mul_f32_e32 v94, v2, v115
	v_mul_f32_e32 v95, v2, v103
	v_mul_f32_e32 v99, v2, v116
	v_mul_f32_e32 v100, v2, v3
	v_mul_f32_e32 v4, v2, v4
	v_mul_f32_e32 v5, v2, v5
	v_max_f32_e64 v2, |v6|, |v7|
	v_max_f32_e64 v3, |v8|, |v9|
	v_max_f32_e64 v98, |v10|, |v11|
	v_max_f32_e64 v101, |v12|, |v13|
	v_max3_f32 v2, v2, 0, v3
	v_max_f32_e64 v102, |v14|, |v15|
	v_max_f32_e64 v103, |v94|, |v95|
	v_max3_f32 v2, v2, v98, v101
	v_max_f32_e64 v104, |v99|, |v100|
	v_max_f32_e64 v105, |v4|, |v5|
	v_max3_f32 v2, v2, v102, v103
	v_max3_f32 v2, v2, v104, v105
	v_mov_b32_e32 v3, v2
	s_nop 1
	v_permlane32_swap_b32 v3, v2
	s_mov_b32 s12, 0x42ee0000
	v_add_u32_e32 v98, s86, v0
	v_cmp_gt_i32_e64 s[48:49], s87, v98
	s_waitcnt lgkmcnt(0)
	v_max_f32_e32 v3, v3, v3
	v_max_f32_e32 v2, v2, v3
	v_mov_b32_e32 v3, v2
	s_nop 1
	v_permlane16_swap_b32 v3, v2
	s_waitcnt lgkmcnt(0)
	v_max_f32_e32 v3, v3, v3
	v_max_f32_e32 v2, v2, v3
	s_nop 1
	v_mov_b32_dpp v3, v2 row_ror:8 row_mask:0xf bank_mask:0xf
	s_waitcnt lgkmcnt(0)
	v_max_f32_e32 v3, v3, v3
	v_max_f32_e32 v2, v2, v3
	s_nop 1
	v_mov_b32_dpp v3, v2 row_half_mirror row_mask:0xf bank_mask:0xf
	s_nop 1
	v_mov_b32_dpp v3, v3 quad_perm:[3,2,1,0] row_mask:0xf bank_mask:0xf
	s_waitcnt lgkmcnt(0)
	v_max_f32_e32 v3, v3, v3
	v_max_f32_e32 v2, v2, v3
	s_nop 1
	v_mov_b32_dpp v3, v2 quad_perm:[2,3,0,1] row_mask:0xf bank_mask:0xf
	s_waitcnt lgkmcnt(0)
	v_max_f32_e32 v3, v3, v3
	v_max_f32_e32 v101, v2, v3
	s_nop 1
	v_mov_b32_dpp v102, v101 quad_perm:[1,0,3,2] row_mask:0xf bank_mask:0xf
	v_lshlrev_b64 v[2:3], 10, v[0:1]
	v_lshl_add_u64 v[206:207], v[2:3], 2, v[44:45]
	global_load_dwordx4 v[208:211], v[206:207], off offset:48
	global_load_dwordx4 v[212:215], v[206:207], off offset:32
	global_load_dwordx4 v[216:219], v[206:207], off offset:16
	global_load_dwordx4 v[220:223], v[206:207], off
	s_waitcnt lgkmcnt(0)
	v_max_f32_e32 v1, v102, v102
	v_max_f32_e32 v101, v101, v1
	v_div_scale_f32 v1, s[10:11], v101, v101, s12
	v_rcp_f32_e32 v102, v1
	v_div_scale_f32 v103, vcc, s12, v101, s12
	s_movk_i32 s10, 0x3fff
	v_fma_f32 v104, -v1, v102, 1.0
	v_fmac_f32_e32 v102, v104, v102
	v_mul_f32_e32 v104, v103, v102
	v_fma_f32 v105, -v1, v104, v103
	v_fmac_f32_e32 v104, v105, v102
	v_fma_f32 v1, -v1, v104, v103
	v_div_fmas_f32 v1, v1, v102, v104
	v_div_fixup_f32 v1, v1, v101, s12
	v_cmp_lt_f32_e32 vcc, 0, v101
	v_cmp_lt_i32_e64 s[50:51], s10, v98
	s_or_b64 s[8:9], s[50:51], s[8:9]
	v_cndmask_b32_e32 v102, 0, v1, vcc
	v_mul_f32_e32 v1, v6, v102
	v_mul_f32_e32 v6, v7, v102
	v_mul_f32_e32 v7, v8, v102
	v_mul_f32_e32 v8, v9, v102
	v_rndne_f32_e32 v1, v1
	v_rndne_f32_e32 v6, v6
	v_mul_f32_e32 v9, v10, v102
	v_mul_f32_e32 v10, v11, v102
	v_rndne_f32_e32 v7, v7
	v_rndne_f32_e32 v8, v8
	v_cvt_i32_f32_e32 v1, v1
	v_cvt_i32_f32_e32 v6, v6
	v_rndne_f32_e32 v9, v9
	v_rndne_f32_e32 v10, v10
	v_cvt_i32_f32_e32 v7, v7
	v_cvt_i32_f32_e32 v8, v8
	v_cvt_i32_f32_e32 v9, v9
	v_cvt_i32_f32_e32 v10, v10
	v_mul_f32_e32 v11, v12, v102
	v_add_u32_e32 v12, 8, v1
	v_add_u32_e32 v104, 8, v6
	v_and_b32_e32 v103, 15, v1
	v_lshlrev_b32_e32 v105, 4, v6
	v_add_u32_e32 v1, v1, v6
	v_lshl_add_u32 v6, v7, 4, v196
	v_lshl_add_u32 v107, v8, 8, v200
	v_lshrrev_b32_e32 v12, 4, v12
	v_and_b32_e32 v104, 0xf0, v104
	v_lshl_add_u32 v109, v9, 12, v201
	v_lshl_add_u32 v111, v10, 16, v202
	v_and_b32_e32 v6, 0xf00, v6
	v_and_b32_e32 v107, 0xf000, v107
	v_and_or_b32 v12, v12, 15, v104
	v_lshlrev_b32_e32 v106, 8, v7
	v_add3_u32 v1, v1, v7, v8
	v_and_b32_e32 v7, 0xf0000, v109
	v_and_b32_e32 v109, 0xf00000, v111
	v_or3_b32 v6, v12, v6, v107
	v_lshlrev_b32_e32 v110, 16, v9
	v_or3_b32 v6, v6, v7, v109
	v_add3_u32 v7, v1, v9, v10
	v_mul_f32_e32 v9, v13, v102
	v_rndne_f32_e32 v11, v11
	v_rndne_f32_e32 v9, v9
	v_cvt_i32_f32_e32 v11, v11
	v_cvt_i32_f32_e32 v9, v9
	v_lshlrev_b32_e32 v108, 12, v8
	v_and_b32_e32 v105, 0xf0, v105
	v_lshl_add_u32 v1, v11, 20, v203
	v_lshl_add_u32 v12, v9, 24, v204
	v_and_b32_e32 v1, 0xf000000, v1
	v_and_b32_e32 v12, 0xf0000000, v12
	v_and_b32_e32 v106, 0xf00, v106
	v_or3_b32 v1, v6, v1, v12
	v_lshl_or_b32 v6, v9, 28, v103
	v_lshlrev_b32_e32 v112, 20, v10
	v_and_b32_e32 v108, 0xf000, v108
	v_and_b32_e32 v8, 0xf0000, v110
	v_lshlrev_b32_e32 v10, 24, v11
	v_or3_b32 v6, v6, v105, v106
	v_and_b32_e32 v110, 0xf00000, v112
	v_and_b32_e32 v10, 0xf000000, v10
	v_or3_b32 v6, v6, v108, v8
	v_or3_b32 v10, v6, v110, v10
	v_add3_u32 v6, v7, v11, v9
	v_mul_f32_e32 v7, v14, v102
	v_mul_f32_e32 v8, v15, v102
	v_rndne_f32_e32 v7, v7
	v_rndne_f32_e32 v8, v8
	v_cvt_i32_f32_e32 v7, v7
	v_cvt_i32_f32_e32 v8, v8
	v_mul_f32_e32 v14, v99, v102
	v_mul_f32_e32 v15, v100, v102
	v_add_u32_e32 v9, 8, v7
	v_add_u32_e32 v11, 8, v8
	v_lshrrev_b32_e32 v9, 4, v9
	v_and_b32_e32 v11, 0xf0, v11
	v_and_or_b32 v9, v9, 15, v11
	v_mul_f32_e32 v11, v94, v102
	v_lshlrev_b32_e32 v13, 4, v8
	v_add3_u32 v6, v6, v7, v8
	v_mul_f32_e32 v8, v95, v102
	v_rndne_f32_e32 v11, v11
	v_rndne_f32_e32 v8, v8
	v_cvt_i32_f32_e32 v11, v11
	v_cvt_i32_f32_e32 v8, v8
	v_rndne_f32_e32 v14, v14
	v_rndne_f32_e32 v15, v15
	v_mul_f32_e32 v4, v4, v102
	v_mul_f32_e32 v5, v5, v102
	v_cvt_i32_f32_e32 v14, v14
	v_cvt_i32_f32_e32 v15, v15
	v_rndne_f32_e32 v4, v4
	v_rndne_f32_e32 v5, v5
	v_cvt_i32_f32_e32 v4, v4
	v_cvt_i32_f32_e32 v5, v5
	v_add3_u32 v6, v6, v11, v8
	v_add3_u32 v6, v6, v14, v15
	v_and_b32_e32 v12, 15, v7
	v_add3_u32 v6, v6, v4, v5
	v_cvt_f32_i32_e32 v6, v6
	v_lshl_add_u32 v7, v11, 4, v196
	v_lshlrev_b32_e32 v11, 8, v11
	v_and_b32_e32 v94, 0xf00, v11
	v_mov_b32_e32 v95, v6
	s_nop 1
	v_permlane32_swap_b32 v95, v6
	v_lshl_add_u32 v11, v8, 8, v200
	v_and_b32_e32 v7, 0xf00, v7
	v_and_b32_e32 v11, 0xf000, v11
	v_or3_b32 v7, v9, v7, v11
	s_waitcnt lgkmcnt(0)
	v_add_f32_e32 v6, v95, v6
	v_mov_b32_e32 v9, v6
	s_nop 1
	v_permlane16_swap_b32 v9, v6
	v_lshl_add_u32 v11, v14, 12, v201
	v_lshl_add_u32 v95, v15, 16, v202
	v_and_b32_e32 v11, 0xf0000, v11
	v_and_b32_e32 v95, 0xf00000, v95
	s_waitcnt lgkmcnt(0)
	v_add_f32_e32 v6, v6, v9
	s_nop 1
	v_mov_b32_dpp v9, v6 row_ror:8 row_mask:0xf bank_mask:0xf
	v_or3_b32 v7, v7, v11, v95
	v_lshlrev_b32_e32 v11, 20, v15
	v_and_b32_e32 v15, 0xf00000, v11
	v_lshl_add_u32 v11, v4, 20, v203
	s_waitcnt lgkmcnt(0)
	v_add_f32_e32 v6, v6, v9
	s_nop 1
	v_mov_b32_dpp v9, v6 row_half_mirror row_mask:0xf bank_mask:0xf
	s_nop 1
	v_mov_b32_dpp v9, v9 quad_perm:[3,2,1,0] row_mask:0xf bank_mask:0xf
	v_lshl_add_u32 v95, v5, 24, v204
	v_and_b32_e32 v11, 0xf000000, v11
	v_and_b32_e32 v95, 0xf0000000, v95
	v_or3_b32 v11, v7, v11, v95
	s_waitcnt lgkmcnt(0)
	v_add_f32_e32 v6, v6, v9
	s_nop 1
	v_mov_b32_dpp v9, v6 quad_perm:[2,3,0,1] row_mask:0xf bank_mask:0xf
	v_and_b32_e32 v13, 0xf0, v13
	v_lshlrev_b32_e32 v8, 12, v8
	v_lshlrev_b32_e32 v14, 16, v14
	v_lshl_or_b32 v5, v5, 28, v12
	s_waitcnt lgkmcnt(0)
	v_add_f32_e32 v6, v6, v9
	s_nop 1
	v_mov_b32_dpp v7, v6 quad_perm:[1,0,3,2] row_mask:0xf bank_mask:0xf
	v_and_b32_e32 v8, 0xf000, v8
	v_and_b32_e32 v14, 0xf0000, v14
	v_lshlrev_b32_e32 v4, 24, v4
	v_or3_b32 v5, v5, v13, v94
	v_and_b32_e32 v4, 0xf000000, v4
	v_or3_b32 v5, v5, v8, v14
	v_or3_b32 v12, v5, v15, v4
	s_waitcnt lgkmcnt(0)
	v_add_f32_e32 v4, v6, v7
	v_mul_f32_e32 v13, 0x3c09ae41, v101
	v_mul_f32_e32 v14, 0.5, v4
	v_mov_b32_e32 v105, 0
	v_mov_b64_e32 v[4:5], v[48:49]
	v_mov_b32_e32 v104, 0
	v_mov_b32_e32 v103, 0
	v_mov_b32_e32 v102, 0
	v_mov_b32_e32 v101, 0
	v_mov_b32_e32 v100, 0
	v_mov_b32_e32 v99, 0
	v_mov_b32_e32 v15, 0
	.p2align 6
